# trailing re-read skip extended to the two GLU K-loops (8 GEMM loops in all)
# baseline (speedup 1.0000x reference)
.LBB0_1854:
	ds_read_b128 v[100:103], v197
	ds_read_b128 v[132:135], v197 offset:1024
	ds_read_b128 v[136:139], v197 offset:2048
	ds_read_b128 v[140:143], v197 offset:3072
	ds_read_b128 v[144:147], v198
	ds_read_b128 v[148:151], v198 offset:1024
	ds_read_b128 v[152:155], v198 offset:2048
	ds_read_b128 v[156:159], v198 offset:3072
	s_add_i32 s53, s21, 2
	s_cmp_eq_u32 s20, 0x9f000
	s_cselect_b32 s59, s48, s51
	s_cselect_b32 s60, 0, s53
	s_cselect_b32 s58, s49, s52
	s_cselect_b64 s[98:99], s[18:19], exec
	s_mov_b64 s[100:101], exec
	s_add_i32 s61, s52, s20
	s_add_u32 s62, s3, s61
	s_addc_u32 s63, s30, 0
	v_lshl_add_u64 v[190:191], s[62:63], 0, v[164:165]
	s_add_i32 m0, s23, 0xc000
	ds_read_b128 v[160:163], v199
	ds_read_b128 v[174:177], v199 offset:1024
	ds_read_b128 v[178:181], v199 offset:2048
	ds_read_b128 v[182:185], v199 offset:3072
	ds_read_b128 v[186:189], v199 offset:4096
	ds_read_b128 v[200:203], v199 offset:5120
	ds_read_b128 v[204:207], v199 offset:6144
	ds_read_b128 v[208:211], v199 offset:7168
	global_load_lds_dwordx4 v[190:191], off
	v_lshl_add_u64 v[190:191], s[62:63], 0, v[166:167]
	s_add_i32 m0, s23, 0xe000
	s_nop 0
	global_load_lds_dwordx4 v[190:191], off
	s_waitcnt vmcnt(8)
	s_waitcnt lgkmcnt(0)
	s_barrier
	s_waitcnt lgkmcnt(0)
	v_mfma_f32_16x16x32_bf16 v[128:131], v[100:103], v[160:163], v[128:131]
	v_mfma_f32_16x16x32_bf16 v[124:127], v[136:139], v[160:163], v[124:127]
	v_mfma_f32_16x16x32_bf16 v[116:119], v[100:103], v[178:181], v[116:119]
	v_mfma_f32_16x16x32_bf16 v[108:111], v[136:139], v[178:181], v[108:111]
	v_mfma_f32_16x16x32_bf16 v[92:95], v[100:103], v[186:189], v[92:95]
	v_mfma_f32_16x16x32_bf16 v[84:87], v[136:139], v[186:189], v[84:87]
	v_mfma_f32_16x16x32_bf16 v[76:79], v[100:103], v[204:207], v[76:79]
	v_mfma_f32_16x16x32_bf16 v[68:71], v[136:139], v[204:207], v[68:71]
	v_mfma_f32_16x16x32_bf16 v[128:131], v[132:135], v[174:177], v[128:131]
	v_mfma_f32_16x16x32_bf16 v[124:127], v[140:143], v[174:177], v[124:127]
	v_mfma_f32_16x16x32_bf16 v[116:119], v[132:135], v[182:185], v[116:119]
	v_mfma_f32_16x16x32_bf16 v[108:111], v[140:143], v[182:185], v[108:111]
	v_mfma_f32_16x16x32_bf16 v[92:95], v[132:135], v[200:203], v[92:95]
	v_mfma_f32_16x16x32_bf16 v[84:87], v[140:143], v[200:203], v[84:87]
	v_mfma_f32_16x16x32_bf16 v[76:79], v[132:135], v[208:211], v[76:79]
	v_mfma_f32_16x16x32_bf16 v[68:71], v[140:143], v[208:211], v[68:71]
	v_mfma_f32_16x16x32_bf16 v[96:99], v[144:147], v[160:163], v[96:99]
	v_mfma_f32_16x16x32_bf16 v[120:123], v[152:155], v[160:163], v[120:123]
	v_mfma_f32_16x16x32_bf16 v[112:115], v[144:147], v[178:181], v[112:115]
	v_mfma_f32_16x16x32_bf16 v[104:107], v[152:155], v[178:181], v[104:107]
	v_mfma_f32_16x16x32_bf16 v[88:91], v[144:147], v[186:189], v[88:91]
	v_mfma_f32_16x16x32_bf16 v[80:83], v[152:155], v[186:189], v[80:83]
	v_mfma_f32_16x16x32_bf16 v[72:75], v[144:147], v[204:207], v[72:75]
	v_mfma_f32_16x16x32_bf16 v[64:67], v[152:155], v[204:207], v[64:67]
	v_mfma_f32_16x16x32_bf16 v[96:99], v[148:151], v[174:177], v[96:99]
	v_mfma_f32_16x16x32_bf16 v[120:123], v[156:159], v[174:177], v[120:123]
	v_mfma_f32_16x16x32_bf16 v[112:115], v[148:151], v[182:185], v[112:115]
	v_mfma_f32_16x16x32_bf16 v[104:107], v[156:159], v[182:185], v[104:107]
	v_mfma_f32_16x16x32_bf16 v[88:91], v[148:151], v[200:203], v[88:91]
	v_mfma_f32_16x16x32_bf16 v[80:83], v[156:159], v[200:203], v[80:83]
	v_mfma_f32_16x16x32_bf16 v[72:75], v[148:151], v[208:211], v[72:75]
	v_mfma_f32_16x16x32_bf16 v[64:67], v[156:159], v[208:211], v[64:67]
	s_barrier
	s_lshl_b32 s61, s60, 7
	s_add_i32 s62, s61, s59
	s_ashr_i32 s63, s62, 31
	s_add_u32 s62, s4, s62
	s_addc_u32 s63, s5, s63
	s_add_i32 s66, s42, s31
	v_lshl_add_u64 v[190:191], s[62:63], 0, v[168:169]
	s_mov_b32 m0, s66
	ds_read_b128 v[160:163], v199 offset:16384
	ds_read_b128 v[174:177], v199 offset:17408
	ds_read_b128 v[178:181], v199 offset:18432
	ds_read_b128 v[182:185], v199 offset:19456
	ds_read_b128 v[186:189], v199 offset:20480
	ds_read_b128 v[200:203], v199 offset:21504
	ds_read_b128 v[204:207], v199 offset:22528
	ds_read_b128 v[208:211], v199 offset:23552
	s_mov_b64 exec, s[98:99]
	global_load_lds_dwordx4 v[190:191], off
	s_add_i32 m0, s66, 0x2000
	s_add_i32 s66, s59, 0x80000
	s_add_i32 s61, s66, s61
	v_lshl_add_u64 v[190:191], s[62:63], 0, v[170:171]
	s_ashr_i32 s63, s61, 31
	s_add_u32 s62, s4, s61
	s_addc_u32 s63, s5, s63
	s_add_i32 s61, s43, s31
	global_load_lds_dwordx4 v[190:191], off
	v_lshl_add_u64 v[190:191], s[62:63], 0, v[168:169]
	s_mov_b32 m0, s61
	s_nop 0
	global_load_lds_dwordx4 v[190:191], off
	s_add_i32 m0, s61, 0x2000
	s_lshl_b32 s61, s60, 12
	s_add_i32 s61, s61, s58
	v_lshl_add_u64 v[190:191], s[62:63], 0, v[170:171]
	s_add_u32 s62, s3, s61
	s_addc_u32 s63, s30, 0
	global_load_lds_dwordx4 v[190:191], off
	v_lshl_add_u64 v[190:191], s[62:63], 0, v[164:165]
	s_mov_b32 m0, s23
	s_nop 0
	global_load_lds_dwordx4 v[190:191], off
	v_lshl_add_u64 v[190:191], s[62:63], 0, v[166:167]
	s_mov_b32 m0, s24
	s_nop 0
	global_load_lds_dwordx4 v[190:191], off
	s_mov_b64 exec, s[100:101]
	s_waitcnt vmcnt(8)
	s_mov_b64 exec, s[98:99]
	s_cbranch_execnz .Lgw_5_42106
	s_waitcnt vmcnt(2)
.Lgw_5_42106:
	s_mov_b64 exec, s[100:101]
	s_waitcnt lgkmcnt(0)
	s_barrier
	s_waitcnt lgkmcnt(0)
	v_mfma_f32_16x16x32_bf16 v[60:63], v[100:103], v[160:163], v[60:63]
	v_mfma_f32_16x16x32_bf16 v[52:55], v[136:139], v[160:163], v[52:55]
	v_mfma_f32_16x16x32_bf16 v[44:47], v[100:103], v[178:181], v[44:47]
	v_mfma_f32_16x16x32_bf16 v[36:39], v[136:139], v[178:181], v[36:39]
	v_mfma_f32_16x16x32_bf16 v[28:31], v[100:103], v[186:189], v[28:31]
	v_mfma_f32_16x16x32_bf16 v[20:23], v[136:139], v[186:189], v[20:23]
	v_mfma_f32_16x16x32_bf16 v[12:15], v[100:103], v[204:207], v[12:15]
	v_mfma_f32_16x16x32_bf16 v[4:7], v[136:139], v[204:207], v[4:7]
	v_mfma_f32_16x16x32_bf16 v[60:63], v[132:135], v[174:177], v[60:63]
	v_mfma_f32_16x16x32_bf16 v[52:55], v[140:143], v[174:177], v[52:55]
	v_mfma_f32_16x16x32_bf16 v[44:47], v[132:135], v[182:185], v[44:47]
	v_mfma_f32_16x16x32_bf16 v[36:39], v[140:143], v[182:185], v[36:39]
	v_mfma_f32_16x16x32_bf16 v[28:31], v[132:135], v[200:203], v[28:31]
	v_mfma_f32_16x16x32_bf16 v[20:23], v[140:143], v[200:203], v[20:23]
	v_mfma_f32_16x16x32_bf16 v[12:15], v[132:135], v[208:211], v[12:15]
	v_mfma_f32_16x16x32_bf16 v[4:7], v[140:143], v[208:211], v[4:7]
	v_mfma_f32_16x16x32_bf16 v[56:59], v[144:147], v[160:163], v[56:59]
	v_mfma_f32_16x16x32_bf16 v[48:51], v[152:155], v[160:163], v[48:51]
	v_mfma_f32_16x16x32_bf16 v[40:43], v[144:147], v[178:181], v[40:43]
	v_mfma_f32_16x16x32_bf16 v[32:35], v[152:155], v[178:181], v[32:35]
	v_mfma_f32_16x16x32_bf16 v[24:27], v[144:147], v[186:189], v[24:27]
	v_mfma_f32_16x16x32_bf16 v[16:19], v[152:155], v[186:189], v[16:19]
	v_mfma_f32_16x16x32_bf16 v[8:11], v[144:147], v[204:207], v[8:11]
	v_mfma_f32_16x16x32_bf16 v[0:3], v[152:155], v[204:207], v[0:3]
	v_mfma_f32_16x16x32_bf16 v[56:59], v[148:151], v[174:177], v[56:59]
	v_mfma_f32_16x16x32_bf16 v[48:51], v[156:159], v[174:177], v[48:51]
	v_mfma_f32_16x16x32_bf16 v[40:43], v[148:151], v[182:185], v[40:43]
	v_mfma_f32_16x16x32_bf16 v[32:35], v[156:159], v[182:185], v[32:35]
	v_mfma_f32_16x16x32_bf16 v[24:27], v[148:151], v[200:203], v[24:27]
	v_mfma_f32_16x16x32_bf16 v[16:19], v[156:159], v[200:203], v[16:19]
	v_mfma_f32_16x16x32_bf16 v[8:11], v[148:151], v[208:211], v[8:11]
	v_mfma_f32_16x16x32_bf16 v[0:3], v[156:159], v[208:211], v[0:3]
	s_barrier
	s_add_i32 s67, 0, 0x18000
	s_add_i32 s68, 0, 0x1c000
	v_add_u32_e32 v140, s67, v195
	v_add_u32_e32 v156, s68, v195
	ds_read_b128 v[100:103], v140
	ds_read_b128 v[132:135], v140 offset:1024
	ds_read_b128 v[136:139], v140 offset:2048
	ds_read_b128 v[140:143], v140 offset:3072
	ds_read_b128 v[144:147], v156
	ds_read_b128 v[148:151], v156 offset:1024
	ds_read_b128 v[152:155], v156 offset:2048
	ds_read_b128 v[156:159], v156 offset:3072
	s_add_i32 s61, s61, 0x80000
	s_add_u32 s62, s3, s61
	s_addc_u32 s63, s30, 0
	s_mov_b32 m0, s25
	v_lshl_add_u64 v[190:191], s[62:63], 0, v[164:165]
	ds_read_b128 v[160:163], v199 offset:32768
	ds_read_b128 v[174:177], v199 offset:33792
	ds_read_b128 v[178:181], v199 offset:34816
	ds_read_b128 v[182:185], v199 offset:35840
	ds_read_b128 v[186:189], v199 offset:36864
	ds_read_b128 v[200:203], v199 offset:37888
	ds_read_b128 v[204:207], v199 offset:38912
	ds_read_b128 v[208:211], v199 offset:39936
	s_mov_b64 exec, s[98:99]
	global_load_lds_dwordx4 v[190:191], off
	v_lshl_add_u64 v[190:191], s[62:63], 0, v[166:167]
	s_mov_b32 m0, s26
	s_nop 0
	global_load_lds_dwordx4 v[190:191], off
	s_mov_b64 exec, s[100:101]
	s_waitcnt vmcnt(8)
	s_mov_b64 exec, s[98:99]
	s_cbranch_execnz .Lgw_5_42179
	s_waitcnt vmcnt(0)
; template <class Epi, class Sched, class Hook = NoHook>
; __device__ __forceinline__ void gemm_phase_w(LAS unsigned char* lds, const Sched& S, const Epi& E, int wave_id, const Hook& HK = Hook()) {
;     ...
;         if constexpr (!SEG2) {
;             for (int tt = 0; tt < nt; tt += 2) {
;                 if constexpr (GATHER) { if (tt == nt - 2) {
;                     if (has_next) { gnxt_00 = S.grow_l(nxt, lds, nbuf, R0) + (unsigned)(C0 * 2); gnxt_01 = S.grow_l(nxt, lds, nbuf, R1) + (unsigned)(C1 * 2); gnxt_10 = S.grow_l(nxt, lds, nbuf, 128 + R0) + (unsigned)(C0 * 2); gnxt_11 = S.grow_l(nxt, lds, nbuf, 128 + R1) + (unsigned)(C1 * 2); }
;                     else { gnxt_00 = gcur_00; gnxt_01 = gcur_01; gnxt_10 = gcur_10; gnxt_11 = gcur_11; } } }
;                 PG_TRIP(tt, false, false, false);
.Lgw_5_42179:
	s_mov_b64 exec, s[100:101]
	s_waitcnt lgkmcnt(0)
	s_barrier
	s_waitcnt lgkmcnt(0)
	v_mfma_f32_16x16x32_bf16 v[128:131], v[100:103], v[160:163], v[128:131]
	v_mfma_f32_16x16x32_bf16 v[124:127], v[136:139], v[160:163], v[124:127]
	v_mfma_f32_16x16x32_bf16 v[116:119], v[100:103], v[178:181], v[116:119]
	v_mfma_f32_16x16x32_bf16 v[108:111], v[136:139], v[178:181], v[108:111]
	v_mfma_f32_16x16x32_bf16 v[92:95], v[100:103], v[186:189], v[92:95]
	v_mfma_f32_16x16x32_bf16 v[84:87], v[136:139], v[186:189], v[84:87]
	v_mfma_f32_16x16x32_bf16 v[76:79], v[100:103], v[204:207], v[76:79]
	v_mfma_f32_16x16x32_bf16 v[68:71], v[136:139], v[204:207], v[68:71]
	v_mfma_f32_16x16x32_bf16 v[128:131], v[132:135], v[174:177], v[128:131]
	v_mfma_f32_16x16x32_bf16 v[124:127], v[140:143], v[174:177], v[124:127]
	v_mfma_f32_16x16x32_bf16 v[116:119], v[132:135], v[182:185], v[116:119]
	v_mfma_f32_16x16x32_bf16 v[108:111], v[140:143], v[182:185], v[108:111]
	v_mfma_f32_16x16x32_bf16 v[92:95], v[132:135], v[200:203], v[92:95]
	v_mfma_f32_16x16x32_bf16 v[84:87], v[140:143], v[200:203], v[84:87]
	v_mfma_f32_16x16x32_bf16 v[76:79], v[132:135], v[208:211], v[76:79]
	v_mfma_f32_16x16x32_bf16 v[68:71], v[140:143], v[208:211], v[68:71]
	v_mfma_f32_16x16x32_bf16 v[96:99], v[144:147], v[160:163], v[96:99]
	v_mfma_f32_16x16x32_bf16 v[120:123], v[152:155], v[160:163], v[120:123]
	v_mfma_f32_16x16x32_bf16 v[112:115], v[144:147], v[178:181], v[112:115]
	v_mfma_f32_16x16x32_bf16 v[104:107], v[152:155], v[178:181], v[104:107]
	v_mfma_f32_16x16x32_bf16 v[88:91], v[144:147], v[186:189], v[88:91]
	v_mfma_f32_16x16x32_bf16 v[80:83], v[152:155], v[186:189], v[80:83]
	v_mfma_f32_16x16x32_bf16 v[72:75], v[144:147], v[204:207], v[72:75]
	v_mfma_f32_16x16x32_bf16 v[64:67], v[152:155], v[204:207], v[64:67]
	v_mfma_f32_16x16x32_bf16 v[96:99], v[148:151], v[174:177], v[96:99]
	v_mfma_f32_16x16x32_bf16 v[120:123], v[156:159], v[174:177], v[120:123]
	v_mfma_f32_16x16x32_bf16 v[112:115], v[148:151], v[182:185], v[112:115]
	v_mfma_f32_16x16x32_bf16 v[104:107], v[156:159], v[182:185], v[104:107]
	v_mfma_f32_16x16x32_bf16 v[88:91], v[148:151], v[200:203], v[88:91]
	v_mfma_f32_16x16x32_bf16 v[80:83], v[156:159], v[200:203], v[80:83]
	v_mfma_f32_16x16x32_bf16 v[72:75], v[148:151], v[208:211], v[72:75]
	v_mfma_f32_16x16x32_bf16 v[64:67], v[156:159], v[208:211], v[64:67]
	s_barrier
	s_or_b32 s62, s60, 1
	s_lshl_b32 s63, s62, 7
	s_add_i32 s59, s63, s59
	s_ashr_i32 s61, s59, 31
	s_add_u32 s60, s4, s59
	s_addc_u32 s61, s5, s61
	s_add_i32 s59, s67, s31
	v_lshl_add_u64 v[190:191], s[60:61], 0, v[168:169]
	s_mov_b32 m0, s59
	s_add_i32 s63, s63, s66
	ds_read_b128 v[160:163], v199 offset:49152
	ds_read_b128 v[174:177], v199 offset:50176
	ds_read_b128 v[178:181], v199 offset:51200
	ds_read_b128 v[182:185], v199 offset:52224
	ds_read_b128 v[186:189], v199 offset:53248
	ds_read_b128 v[200:203], v199 offset:54272
	ds_read_b128 v[204:207], v199 offset:55296
	ds_read_b128 v[208:211], v199 offset:56320
	s_mov_b64 exec, s[98:99]
	global_load_lds_dwordx4 v[190:191], off
	s_add_i32 m0, s59, 0x2000
	s_ashr_i32 s59, s63, 31
	v_lshl_add_u64 v[190:191], s[60:61], 0, v[170:171]
	s_add_u32 s60, s4, s63
	s_addc_u32 s61, s5, s59
	s_add_i32 s59, s68, s31
	global_load_lds_dwordx4 v[190:191], off
	v_lshl_add_u64 v[190:191], s[60:61], 0, v[168:169]
	s_mov_b32 m0, s59
	s_nop 0
	global_load_lds_dwordx4 v[190:191], off
	s_add_i32 m0, s59, 0x2000
	s_lshl_b32 s59, s62, 12
	s_add_i32 s59, s59, s58
	s_add_u32 s58, s3, s59
	v_lshl_add_u64 v[190:191], s[60:61], 0, v[170:171]
	s_addc_u32 s59, s30, 0
	global_load_lds_dwordx4 v[190:191], off
	v_lshl_add_u64 v[190:191], s[58:59], 0, v[164:165]
	s_mov_b32 m0, s28
	s_nop 0
	global_load_lds_dwordx4 v[190:191], off
	v_lshl_add_u64 v[190:191], s[58:59], 0, v[166:167]
	s_mov_b32 m0, s29
	s_nop 0
	global_load_lds_dwordx4 v[190:191], off
	s_mov_b64 exec, s[100:101]
	s_waitcnt vmcnt(8)
	s_mov_b64 exec, s[98:99]
	s_cbranch_execnz .Lgw_5_42266
	s_waitcnt vmcnt(0)
.Lgw_5_42266:
	s_mov_b64 exec, s[100:101]
	s_waitcnt lgkmcnt(0)
	s_barrier
	s_waitcnt lgkmcnt(0)
	v_mfma_f32_16x16x32_bf16 v[60:63], v[100:103], v[160:163], v[60:63]
	v_mfma_f32_16x16x32_bf16 v[52:55], v[136:139], v[160:163], v[52:55]
	v_mfma_f32_16x16x32_bf16 v[44:47], v[100:103], v[178:181], v[44:47]
	v_mfma_f32_16x16x32_bf16 v[36:39], v[136:139], v[178:181], v[36:39]
	v_mfma_f32_16x16x32_bf16 v[28:31], v[100:103], v[186:189], v[28:31]
	v_mfma_f32_16x16x32_bf16 v[20:23], v[136:139], v[186:189], v[20:23]
	v_mfma_f32_16x16x32_bf16 v[12:15], v[100:103], v[204:207], v[12:15]
	v_mfma_f32_16x16x32_bf16 v[4:7], v[136:139], v[204:207], v[4:7]
	v_mfma_f32_16x16x32_bf16 v[60:63], v[132:135], v[174:177], v[60:63]
	v_mfma_f32_16x16x32_bf16 v[52:55], v[140:143], v[174:177], v[52:55]
	v_mfma_f32_16x16x32_bf16 v[44:47], v[132:135], v[182:185], v[44:47]
	v_mfma_f32_16x16x32_bf16 v[36:39], v[140:143], v[182:185], v[36:39]
	v_mfma_f32_16x16x32_bf16 v[28:31], v[132:135], v[200:203], v[28:31]
	v_mfma_f32_16x16x32_bf16 v[20:23], v[140:143], v[200:203], v[20:23]
	v_mfma_f32_16x16x32_bf16 v[12:15], v[132:135], v[208:211], v[12:15]
	v_mfma_f32_16x16x32_bf16 v[4:7], v[140:143], v[208:211], v[4:7]
	v_mfma_f32_16x16x32_bf16 v[56:59], v[144:147], v[160:163], v[56:59]
	v_mfma_f32_16x16x32_bf16 v[48:51], v[152:155], v[160:163], v[48:51]
	v_mfma_f32_16x16x32_bf16 v[40:43], v[144:147], v[178:181], v[40:43]
	v_mfma_f32_16x16x32_bf16 v[32:35], v[152:155], v[178:181], v[32:35]
	v_mfma_f32_16x16x32_bf16 v[24:27], v[144:147], v[186:189], v[24:27]
	v_mfma_f32_16x16x32_bf16 v[16:19], v[152:155], v[186:189], v[16:19]
	v_mfma_f32_16x16x32_bf16 v[8:11], v[144:147], v[204:207], v[8:11]
	v_mfma_f32_16x16x32_bf16 v[0:3], v[152:155], v[204:207], v[0:3]
	v_mfma_f32_16x16x32_bf16 v[56:59], v[148:151], v[174:177], v[56:59]
	v_mfma_f32_16x16x32_bf16 v[48:51], v[156:159], v[174:177], v[48:51]
	v_mfma_f32_16x16x32_bf16 v[40:43], v[148:151], v[182:185], v[40:43]
	v_mfma_f32_16x16x32_bf16 v[32:35], v[156:159], v[182:185], v[32:35]
	v_mfma_f32_16x16x32_bf16 v[24:27], v[148:151], v[200:203], v[24:27]
	v_mfma_f32_16x16x32_bf16 v[16:19], v[156:159], v[200:203], v[16:19]
	v_mfma_f32_16x16x32_bf16 v[8:11], v[148:151], v[208:211], v[8:11]
	v_mfma_f32_16x16x32_bf16 v[0:3], v[156:159], v[208:211], v[0:3]
	s_barrier
	s_addk_i32 s20, 0x2000
	s_cmp_gt_u32 s21, 29
	s_mov_b32 s21, s53
	s_cbranch_scc0 .LBB0_1854
	s_and_b64 vcc, exec, s[16:17]
	s_cbranch_vccz .LBB0_1857
	s_barrier

.LBB0_1983:
	ds_read_b128 v[100:103], v195
	ds_read_b128 v[132:135], v195 offset:1024
	ds_read_b128 v[136:139], v195 offset:2048
	ds_read_b128 v[140:143], v195 offset:3072
	ds_read_b128 v[144:147], v196
	ds_read_b128 v[148:151], v196 offset:1024
	ds_read_b128 v[152:155], v196 offset:2048
	ds_read_b128 v[156:159], v196 offset:3072
	s_add_i32 s45, s21, 2
	s_cmp_eq_u32 s20, 0x9f000
	s_cselect_b32 s49, s40, s43
	s_cselect_b32 s50, 0, s45
	s_cselect_b32 s48, s41, s44
	s_cselect_b64 s[98:99], s[18:19], exec
	s_mov_b64 s[100:101], exec
	s_add_i32 s51, s44, s20
	s_add_u32 s52, s3, s51
	s_addc_u32 s53, s30, 0
	v_lshl_add_u64 v[190:191], s[52:53], 0, v[164:165]
	s_add_i32 m0, s24, 0xc000
	ds_read_b128 v[160:163], v197
	ds_read_b128 v[174:177], v197 offset:1024
	ds_read_b128 v[178:181], v197 offset:2048
	ds_read_b128 v[182:185], v197 offset:3072
	ds_read_b128 v[186:189], v197 offset:4096
	ds_read_b128 v[198:201], v197 offset:5120
	ds_read_b128 v[202:205], v197 offset:6144
	ds_read_b128 v[206:209], v197 offset:7168
	global_load_lds_dwordx4 v[190:191], off
	v_lshl_add_u64 v[190:191], s[52:53], 0, v[166:167]
	s_add_i32 m0, s24, 0xe000
	s_nop 0
	global_load_lds_dwordx4 v[190:191], off
	s_waitcnt vmcnt(8)
	s_waitcnt lgkmcnt(0)
	s_barrier
	s_waitcnt lgkmcnt(0)
	v_mfma_f32_16x16x32_bf16 v[128:131], v[100:103], v[160:163], v[128:131]
	v_mfma_f32_16x16x32_bf16 v[124:127], v[136:139], v[160:163], v[124:127]
	v_mfma_f32_16x16x32_bf16 v[116:119], v[100:103], v[178:181], v[116:119]
	v_mfma_f32_16x16x32_bf16 v[108:111], v[136:139], v[178:181], v[108:111]
	v_mfma_f32_16x16x32_bf16 v[92:95], v[100:103], v[186:189], v[92:95]
	v_mfma_f32_16x16x32_bf16 v[84:87], v[136:139], v[186:189], v[84:87]
	v_mfma_f32_16x16x32_bf16 v[76:79], v[100:103], v[202:205], v[76:79]
	v_mfma_f32_16x16x32_bf16 v[68:71], v[136:139], v[202:205], v[68:71]
	v_mfma_f32_16x16x32_bf16 v[128:131], v[132:135], v[174:177], v[128:131]
	v_mfma_f32_16x16x32_bf16 v[124:127], v[140:143], v[174:177], v[124:127]
	v_mfma_f32_16x16x32_bf16 v[116:119], v[132:135], v[182:185], v[116:119]
	v_mfma_f32_16x16x32_bf16 v[108:111], v[140:143], v[182:185], v[108:111]
	v_mfma_f32_16x16x32_bf16 v[92:95], v[132:135], v[198:201], v[92:95]
	v_mfma_f32_16x16x32_bf16 v[84:87], v[140:143], v[198:201], v[84:87]
	v_mfma_f32_16x16x32_bf16 v[76:79], v[132:135], v[206:209], v[76:79]
	v_mfma_f32_16x16x32_bf16 v[68:71], v[140:143], v[206:209], v[68:71]
	v_mfma_f32_16x16x32_bf16 v[96:99], v[144:147], v[160:163], v[96:99]
	v_mfma_f32_16x16x32_bf16 v[120:123], v[152:155], v[160:163], v[120:123]
	v_mfma_f32_16x16x32_bf16 v[112:115], v[144:147], v[178:181], v[112:115]
	v_mfma_f32_16x16x32_bf16 v[104:107], v[152:155], v[178:181], v[104:107]
	v_mfma_f32_16x16x32_bf16 v[88:91], v[144:147], v[186:189], v[88:91]
	v_mfma_f32_16x16x32_bf16 v[80:83], v[152:155], v[186:189], v[80:83]
	v_mfma_f32_16x16x32_bf16 v[72:75], v[144:147], v[202:205], v[72:75]
	v_mfma_f32_16x16x32_bf16 v[64:67], v[152:155], v[202:205], v[64:67]
	v_mfma_f32_16x16x32_bf16 v[96:99], v[148:151], v[174:177], v[96:99]
	v_mfma_f32_16x16x32_bf16 v[120:123], v[156:159], v[174:177], v[120:123]
	v_mfma_f32_16x16x32_bf16 v[112:115], v[148:151], v[182:185], v[112:115]
	v_mfma_f32_16x16x32_bf16 v[104:107], v[156:159], v[182:185], v[104:107]
	v_mfma_f32_16x16x32_bf16 v[88:91], v[148:151], v[198:201], v[88:91]
	v_mfma_f32_16x16x32_bf16 v[80:83], v[156:159], v[198:201], v[80:83]
	v_mfma_f32_16x16x32_bf16 v[72:75], v[148:151], v[206:209], v[72:75]
	v_mfma_f32_16x16x32_bf16 v[64:67], v[156:159], v[206:209], v[64:67]
	s_barrier
	s_lshl_b32 s51, s50, 7
	s_add_i32 s52, s51, s49
	s_ashr_i32 s53, s52, 31
	s_add_u32 s52, s4, s52
	s_addc_u32 s53, s5, s53
	s_add_i32 s58, s34, s31
	v_lshl_add_u64 v[190:191], s[52:53], 0, v[168:169]
	s_mov_b32 m0, s58
	ds_read_b128 v[160:163], v197 offset:16384
	ds_read_b128 v[174:177], v197 offset:17408
	ds_read_b128 v[178:181], v197 offset:18432
	ds_read_b128 v[182:185], v197 offset:19456
	ds_read_b128 v[186:189], v197 offset:20480
	ds_read_b128 v[198:201], v197 offset:21504
	ds_read_b128 v[202:205], v197 offset:22528
	ds_read_b128 v[206:209], v197 offset:23552
	s_mov_b64 exec, s[98:99]
	global_load_lds_dwordx4 v[190:191], off
	s_add_i32 m0, s58, 0x2000
	s_add_i32 s58, s49, 0x80000
	s_add_i32 s51, s58, s51
	v_lshl_add_u64 v[190:191], s[52:53], 0, v[170:171]
	s_ashr_i32 s53, s51, 31
	s_add_u32 s52, s4, s51
	s_addc_u32 s53, s5, s53
	s_add_i32 s51, s36, s31
	global_load_lds_dwordx4 v[190:191], off
	v_lshl_add_u64 v[190:191], s[52:53], 0, v[168:169]
	s_mov_b32 m0, s51
	s_nop 0
	global_load_lds_dwordx4 v[190:191], off
	s_add_i32 m0, s51, 0x2000
	s_lshl_b32 s51, s50, 12
	s_add_i32 s51, s51, s48
	v_lshl_add_u64 v[190:191], s[52:53], 0, v[170:171]
	s_add_u32 s52, s3, s51
	s_addc_u32 s53, s30, 0
	global_load_lds_dwordx4 v[190:191], off
	v_lshl_add_u64 v[190:191], s[52:53], 0, v[164:165]
	s_mov_b32 m0, s24
	s_nop 0
	global_load_lds_dwordx4 v[190:191], off
	v_lshl_add_u64 v[190:191], s[52:53], 0, v[166:167]
	s_mov_b32 m0, s25
	s_nop 0
	global_load_lds_dwordx4 v[190:191], off
	s_mov_b64 exec, s[100:101]
	s_waitcnt vmcnt(8)
	s_mov_b64 exec, s[98:99]
	s_cbranch_execnz .Lgw_6_45060
	s_waitcnt vmcnt(2)
.Lgw_6_45060:
	s_mov_b64 exec, s[100:101]
	s_waitcnt lgkmcnt(0)
	s_barrier
	s_waitcnt lgkmcnt(0)
	v_mfma_f32_16x16x32_bf16 v[60:63], v[100:103], v[160:163], v[60:63]
	v_mfma_f32_16x16x32_bf16 v[52:55], v[136:139], v[160:163], v[52:55]
	v_mfma_f32_16x16x32_bf16 v[44:47], v[100:103], v[178:181], v[44:47]
	v_mfma_f32_16x16x32_bf16 v[36:39], v[136:139], v[178:181], v[36:39]
	v_mfma_f32_16x16x32_bf16 v[28:31], v[100:103], v[186:189], v[28:31]
	v_mfma_f32_16x16x32_bf16 v[20:23], v[136:139], v[186:189], v[20:23]
	v_mfma_f32_16x16x32_bf16 v[12:15], v[100:103], v[202:205], v[12:15]
	v_mfma_f32_16x16x32_bf16 v[4:7], v[136:139], v[202:205], v[4:7]
	v_mfma_f32_16x16x32_bf16 v[60:63], v[132:135], v[174:177], v[60:63]
	v_mfma_f32_16x16x32_bf16 v[52:55], v[140:143], v[174:177], v[52:55]
	v_mfma_f32_16x16x32_bf16 v[44:47], v[132:135], v[182:185], v[44:47]
	v_mfma_f32_16x16x32_bf16 v[36:39], v[140:143], v[182:185], v[36:39]
	v_mfma_f32_16x16x32_bf16 v[28:31], v[132:135], v[198:201], v[28:31]
	v_mfma_f32_16x16x32_bf16 v[20:23], v[140:143], v[198:201], v[20:23]
	v_mfma_f32_16x16x32_bf16 v[12:15], v[132:135], v[206:209], v[12:15]
	v_mfma_f32_16x16x32_bf16 v[4:7], v[140:143], v[206:209], v[4:7]
	v_mfma_f32_16x16x32_bf16 v[56:59], v[144:147], v[160:163], v[56:59]
	v_mfma_f32_16x16x32_bf16 v[48:51], v[152:155], v[160:163], v[48:51]
	v_mfma_f32_16x16x32_bf16 v[40:43], v[144:147], v[178:181], v[40:43]
	v_mfma_f32_16x16x32_bf16 v[32:35], v[152:155], v[178:181], v[32:35]
	v_mfma_f32_16x16x32_bf16 v[24:27], v[144:147], v[186:189], v[24:27]
	v_mfma_f32_16x16x32_bf16 v[16:19], v[152:155], v[186:189], v[16:19]
	v_mfma_f32_16x16x32_bf16 v[8:11], v[144:147], v[202:205], v[8:11]
	v_mfma_f32_16x16x32_bf16 v[0:3], v[152:155], v[202:205], v[0:3]
	v_mfma_f32_16x16x32_bf16 v[56:59], v[148:151], v[174:177], v[56:59]
	v_mfma_f32_16x16x32_bf16 v[48:51], v[156:159], v[174:177], v[48:51]
	v_mfma_f32_16x16x32_bf16 v[40:43], v[148:151], v[182:185], v[40:43]
	v_mfma_f32_16x16x32_bf16 v[32:35], v[156:159], v[182:185], v[32:35]
	v_mfma_f32_16x16x32_bf16 v[24:27], v[148:151], v[198:201], v[24:27]
	v_mfma_f32_16x16x32_bf16 v[16:19], v[156:159], v[198:201], v[16:19]
	v_mfma_f32_16x16x32_bf16 v[8:11], v[148:151], v[206:209], v[8:11]
	v_mfma_f32_16x16x32_bf16 v[0:3], v[156:159], v[206:209], v[0:3]
	s_barrier
	s_add_i32 s59, 0, 0x18000
	s_add_i32 s60, 0, 0x1c000
	v_add_u32_e32 v140, s59, v193
	v_add_u32_e32 v156, s60, v193
	ds_read_b128 v[100:103], v140
	ds_read_b128 v[132:135], v140 offset:1024
	ds_read_b128 v[136:139], v140 offset:2048
	ds_read_b128 v[140:143], v140 offset:3072
	ds_read_b128 v[144:147], v156
	ds_read_b128 v[148:151], v156 offset:1024
	ds_read_b128 v[152:155], v156 offset:2048
	ds_read_b128 v[156:159], v156 offset:3072
	s_add_i32 s51, s51, 0x80000
	s_add_u32 s52, s3, s51
	s_addc_u32 s53, s30, 0
	s_mov_b32 m0, s26
	v_lshl_add_u64 v[190:191], s[52:53], 0, v[164:165]
	ds_read_b128 v[160:163], v197 offset:32768
	ds_read_b128 v[174:177], v197 offset:33792
	ds_read_b128 v[178:181], v197 offset:34816
	ds_read_b128 v[182:185], v197 offset:35840
	ds_read_b128 v[186:189], v197 offset:36864
	ds_read_b128 v[198:201], v197 offset:37888
	ds_read_b128 v[202:205], v197 offset:38912
	ds_read_b128 v[206:209], v197 offset:39936
	s_mov_b64 exec, s[98:99]
	global_load_lds_dwordx4 v[190:191], off
	v_lshl_add_u64 v[190:191], s[52:53], 0, v[166:167]
	s_mov_b32 m0, s27
	s_nop 0
	global_load_lds_dwordx4 v[190:191], off
	s_mov_b64 exec, s[100:101]
	s_waitcnt vmcnt(8)
	s_mov_b64 exec, s[98:99]
	s_cbranch_execnz .Lgw_6_45133
	s_waitcnt vmcnt(0)
; template <class Epi, class Sched, class Hook = NoHook>
; __device__ __forceinline__ void gemm_phase_w(LAS unsigned char* lds, const Sched& S, const Epi& E, int wave_id, const Hook& HK = Hook()) {
;     ...
;         if constexpr (!SEG2) {
;             for (int tt = 0; tt < nt; tt += 2) {
;                 if constexpr (GATHER) { if (tt == nt - 2) {
;                     if (has_next) { gnxt_00 = S.grow_l(nxt, lds, nbuf, R0) + (unsigned)(C0 * 2); gnxt_01 = S.grow_l(nxt, lds, nbuf, R1) + (unsigned)(C1 * 2); gnxt_10 = S.grow_l(nxt, lds, nbuf, 128 + R0) + (unsigned)(C0 * 2); gnxt_11 = S.grow_l(nxt, lds, nbuf, 128 + R1) + (unsigned)(C1 * 2); }
;                     else { gnxt_00 = gcur_00; gnxt_01 = gcur_01; gnxt_10 = gcur_10; gnxt_11 = gcur_11; } } }
;                 PG_TRIP(tt, false, false, false);
.Lgw_6_45133:
	s_mov_b64 exec, s[100:101]
	s_waitcnt lgkmcnt(0)
	s_barrier
	s_waitcnt lgkmcnt(0)
	v_mfma_f32_16x16x32_bf16 v[128:131], v[100:103], v[160:163], v[128:131]
	v_mfma_f32_16x16x32_bf16 v[124:127], v[136:139], v[160:163], v[124:127]
	v_mfma_f32_16x16x32_bf16 v[116:119], v[100:103], v[178:181], v[116:119]
	v_mfma_f32_16x16x32_bf16 v[108:111], v[136:139], v[178:181], v[108:111]
	v_mfma_f32_16x16x32_bf16 v[92:95], v[100:103], v[186:189], v[92:95]
	v_mfma_f32_16x16x32_bf16 v[84:87], v[136:139], v[186:189], v[84:87]
	v_mfma_f32_16x16x32_bf16 v[76:79], v[100:103], v[202:205], v[76:79]
	v_mfma_f32_16x16x32_bf16 v[68:71], v[136:139], v[202:205], v[68:71]
	v_mfma_f32_16x16x32_bf16 v[128:131], v[132:135], v[174:177], v[128:131]
	v_mfma_f32_16x16x32_bf16 v[124:127], v[140:143], v[174:177], v[124:127]
	v_mfma_f32_16x16x32_bf16 v[116:119], v[132:135], v[182:185], v[116:119]
	v_mfma_f32_16x16x32_bf16 v[108:111], v[140:143], v[182:185], v[108:111]
	v_mfma_f32_16x16x32_bf16 v[92:95], v[132:135], v[198:201], v[92:95]
	v_mfma_f32_16x16x32_bf16 v[84:87], v[140:143], v[198:201], v[84:87]
	v_mfma_f32_16x16x32_bf16 v[76:79], v[132:135], v[206:209], v[76:79]
	v_mfma_f32_16x16x32_bf16 v[68:71], v[140:143], v[206:209], v[68:71]
	v_mfma_f32_16x16x32_bf16 v[96:99], v[144:147], v[160:163], v[96:99]
	v_mfma_f32_16x16x32_bf16 v[120:123], v[152:155], v[160:163], v[120:123]
	v_mfma_f32_16x16x32_bf16 v[112:115], v[144:147], v[178:181], v[112:115]
	v_mfma_f32_16x16x32_bf16 v[104:107], v[152:155], v[178:181], v[104:107]
	v_mfma_f32_16x16x32_bf16 v[88:91], v[144:147], v[186:189], v[88:91]
	v_mfma_f32_16x16x32_bf16 v[80:83], v[152:155], v[186:189], v[80:83]
	v_mfma_f32_16x16x32_bf16 v[72:75], v[144:147], v[202:205], v[72:75]
	v_mfma_f32_16x16x32_bf16 v[64:67], v[152:155], v[202:205], v[64:67]
	v_mfma_f32_16x16x32_bf16 v[96:99], v[148:151], v[174:177], v[96:99]
	v_mfma_f32_16x16x32_bf16 v[120:123], v[156:159], v[174:177], v[120:123]
	v_mfma_f32_16x16x32_bf16 v[112:115], v[148:151], v[182:185], v[112:115]
	v_mfma_f32_16x16x32_bf16 v[104:107], v[156:159], v[182:185], v[104:107]
	v_mfma_f32_16x16x32_bf16 v[88:91], v[148:151], v[198:201], v[88:91]
	v_mfma_f32_16x16x32_bf16 v[80:83], v[156:159], v[198:201], v[80:83]
	v_mfma_f32_16x16x32_bf16 v[72:75], v[148:151], v[206:209], v[72:75]
	v_mfma_f32_16x16x32_bf16 v[64:67], v[156:159], v[206:209], v[64:67]
	s_barrier
	s_or_b32 s52, s50, 1
	s_lshl_b32 s53, s52, 7
	s_add_i32 s49, s53, s49
	s_ashr_i32 s51, s49, 31
	s_add_u32 s50, s4, s49
	s_addc_u32 s51, s5, s51
	s_add_i32 s49, s59, s31
	v_lshl_add_u64 v[190:191], s[50:51], 0, v[168:169]
	s_mov_b32 m0, s49
	s_add_i32 s53, s53, s58
	ds_read_b128 v[160:163], v197 offset:49152
	ds_read_b128 v[174:177], v197 offset:50176
	ds_read_b128 v[178:181], v197 offset:51200
	ds_read_b128 v[182:185], v197 offset:52224
	ds_read_b128 v[186:189], v197 offset:53248
	ds_read_b128 v[198:201], v197 offset:54272
	ds_read_b128 v[202:205], v197 offset:55296
	ds_read_b128 v[206:209], v197 offset:56320
	s_mov_b64 exec, s[98:99]
	global_load_lds_dwordx4 v[190:191], off
	s_add_i32 m0, s49, 0x2000
	s_ashr_i32 s49, s53, 31
	v_lshl_add_u64 v[190:191], s[50:51], 0, v[170:171]
	s_add_u32 s50, s4, s53
	s_addc_u32 s51, s5, s49
	s_add_i32 s49, s60, s31
	global_load_lds_dwordx4 v[190:191], off
	v_lshl_add_u64 v[190:191], s[50:51], 0, v[168:169]
	s_mov_b32 m0, s49
	s_nop 0
	global_load_lds_dwordx4 v[190:191], off
	s_add_i32 m0, s49, 0x2000
	s_lshl_b32 s49, s52, 12
	s_add_i32 s49, s49, s48
	s_add_u32 s48, s3, s49
	v_lshl_add_u64 v[190:191], s[50:51], 0, v[170:171]
	s_addc_u32 s49, s30, 0
	global_load_lds_dwordx4 v[190:191], off
	v_lshl_add_u64 v[190:191], s[48:49], 0, v[164:165]
	s_mov_b32 m0, s29
	s_nop 0
	global_load_lds_dwordx4 v[190:191], off
	v_lshl_add_u64 v[190:191], s[48:49], 0, v[166:167]
	s_mov_b32 m0, s38
	s_nop 0
	global_load_lds_dwordx4 v[190:191], off
	s_mov_b64 exec, s[100:101]
	s_waitcnt vmcnt(8)
	s_mov_b64 exec, s[98:99]
	s_cbranch_execnz .Lgw_6_45220
	s_waitcnt vmcnt(0)
.Lgw_6_45220:
	s_mov_b64 exec, s[100:101]
	s_waitcnt lgkmcnt(0)
	s_barrier
	s_waitcnt lgkmcnt(0)
	v_mfma_f32_16x16x32_bf16 v[60:63], v[100:103], v[160:163], v[60:63]
	v_mfma_f32_16x16x32_bf16 v[52:55], v[136:139], v[160:163], v[52:55]
	v_mfma_f32_16x16x32_bf16 v[44:47], v[100:103], v[178:181], v[44:47]
	v_mfma_f32_16x16x32_bf16 v[36:39], v[136:139], v[178:181], v[36:39]
	v_mfma_f32_16x16x32_bf16 v[28:31], v[100:103], v[186:189], v[28:31]
	v_mfma_f32_16x16x32_bf16 v[20:23], v[136:139], v[186:189], v[20:23]
	v_mfma_f32_16x16x32_bf16 v[12:15], v[100:103], v[202:205], v[12:15]
	v_mfma_f32_16x16x32_bf16 v[4:7], v[136:139], v[202:205], v[4:7]
	v_mfma_f32_16x16x32_bf16 v[60:63], v[132:135], v[174:177], v[60:63]
	v_mfma_f32_16x16x32_bf16 v[52:55], v[140:143], v[174:177], v[52:55]
	v_mfma_f32_16x16x32_bf16 v[44:47], v[132:135], v[182:185], v[44:47]
	v_mfma_f32_16x16x32_bf16 v[36:39], v[140:143], v[182:185], v[36:39]
	v_mfma_f32_16x16x32_bf16 v[28:31], v[132:135], v[198:201], v[28:31]
	v_mfma_f32_16x16x32_bf16 v[20:23], v[140:143], v[198:201], v[20:23]
	v_mfma_f32_16x16x32_bf16 v[12:15], v[132:135], v[206:209], v[12:15]
	v_mfma_f32_16x16x32_bf16 v[4:7], v[140:143], v[206:209], v[4:7]
	v_mfma_f32_16x16x32_bf16 v[56:59], v[144:147], v[160:163], v[56:59]
	v_mfma_f32_16x16x32_bf16 v[48:51], v[152:155], v[160:163], v[48:51]
	v_mfma_f32_16x16x32_bf16 v[40:43], v[144:147], v[178:181], v[40:43]
	v_mfma_f32_16x16x32_bf16 v[32:35], v[152:155], v[178:181], v[32:35]
	v_mfma_f32_16x16x32_bf16 v[24:27], v[144:147], v[186:189], v[24:27]
	v_mfma_f32_16x16x32_bf16 v[16:19], v[152:155], v[186:189], v[16:19]
	v_mfma_f32_16x16x32_bf16 v[8:11], v[144:147], v[202:205], v[8:11]
	v_mfma_f32_16x16x32_bf16 v[0:3], v[152:155], v[202:205], v[0:3]
	v_mfma_f32_16x16x32_bf16 v[56:59], v[148:151], v[174:177], v[56:59]
	v_mfma_f32_16x16x32_bf16 v[48:51], v[156:159], v[174:177], v[48:51]
	v_mfma_f32_16x16x32_bf16 v[40:43], v[148:151], v[182:185], v[40:43]
	v_mfma_f32_16x16x32_bf16 v[32:35], v[156:159], v[182:185], v[32:35]
	v_mfma_f32_16x16x32_bf16 v[24:27], v[148:151], v[198:201], v[24:27]
	v_mfma_f32_16x16x32_bf16 v[16:19], v[156:159], v[198:201], v[16:19]
	v_mfma_f32_16x16x32_bf16 v[8:11], v[148:151], v[206:209], v[8:11]
	v_mfma_f32_16x16x32_bf16 v[0:3], v[156:159], v[206:209], v[0:3]
	s_barrier
	s_addk_i32 s20, 0x2000
	s_cmp_gt_u32 s21, 29
	s_mov_b32 s21, s45
	s_cbranch_scc0 .LBB0_1983
	s_and_b64 vcc, exec, s[16:17]
	s_cbranch_vccz .LBB0_1986
	s_barrier
